# speedup vs baseline: 1.0236x; 1.0236x over previous
.LBB0_10:
	v_cvt_pk_bf16_f32 v17, v16, v17
	v_cvt_pk_bf16_f32 v16, v14, v15
	v_and_b32_e32 v15, 0x7c, v127
	s_movk_i32 s8, 0x110
	v_lshlrev_b32_e32 v15, 1, v15
	v_cvt_pk_bf16_f32 v13, v12, v13
	v_cvt_pk_bf16_f32 v12, v10, v11
	v_mad_u32_u24 v10, v45, s8, v15
	v_cvt_pk_bf16_f32 v5, v4, v5
	v_cvt_pk_bf16_f32 v4, v2, v3
	v_mad_u32_u24 v2, v44, s8, v15
	ds_write_b64 v10, v[12:13]
	ds_write_b64 v2, v[4:5]
	v_cvt_pk_bf16_f32 v3, v24, v25
	v_cvt_pk_bf16_f32 v2, v22, v23
	v_mad_u32_u24 v4, v43, s8, v15
	ds_write_b64 v4, v[2:3]
	v_cvt_pk_bf16_f32 v3, v8, v9
	v_cvt_pk_bf16_f32 v2, v6, v7
	v_mad_u32_u24 v4, v42, s8, v15
	ds_write_b64 v4, v[2:3]
	v_cvt_pk_bf16_f32 v3, v32, v33
	v_cvt_pk_bf16_f32 v2, v30, v31
	v_mad_u32_u24 v4, v41, s8, v15
	ds_write_b64 v4, v[2:3]
	v_cvt_pk_bf16_f32 v3, v20, v21
	v_cvt_pk_bf16_f32 v2, v18, v19
	v_mad_u32_u24 v4, v40, s8, v15
	ds_write_b64 v4, v[2:3]
	v_cvt_pk_bf16_f32 v3, v36, v37
	v_cvt_pk_bf16_f32 v2, v34, v35
	v_mad_u32_u24 v4, v39, s8, v15
	ds_write_b64 v4, v[2:3]
	v_cvt_pk_bf16_f32 v3, v28, v29
	v_cvt_pk_bf16_f32 v2, v26, v27
	v_mad_u32_u24 v4, v38, s8, v15
	v_lshrrev_b32_e32 v14, 5, v0
	ds_write_b64 v4, v[2:3]
	v_mul_u32_u24_e32 v14, 0x110, v14
	s_mov_b32 s9, 0x1b400
	s_waitcnt lgkmcnt(0)
	v_mov_b32_e32 v109, 0
	v_add3_u32 v14, v14, v15, s9
	ds_write_b64 v14, v[16:17]
	s_waitcnt lgkmcnt(0)
	s_barrier
	s_and_b64 vcc, exec, s[6:7]
	s_cbranch_vccnz .Lp_nomask
	v_lshl_add_u32 v102, v128, 1, s12
	v_lshlrev_b32_e32 v102, 12, v102
	v_lshl_add_u32 v102, v126, 4, v102
	v_add_u32_e32 v103, 0x1000, v102
	global_load_dwordx4 v[70:73], v102, s[26:27] nt
	global_load_dwordx4 v[74:77], v102, s[26:27] offset:1024 nt
	global_load_dwordx4 v[78:81], v102, s[26:27] offset:2048 nt
	global_load_dwordx4 v[82:85], v102, s[26:27] offset:3072 nt
	global_load_dwordx4 v[86:89], v103, s[26:27] nt
	global_load_dwordx4 v[90:93], v103, s[26:27] offset:1024 nt
	global_load_dwordx4 v[94:97], v103, s[26:27] offset:2048 nt
	global_load_dwordx4 v[98:101], v103, s[26:27] offset:3072 nt
.Lp_nomask:
	s_andn2_b64 vcc, exec, s[6:7]
	s_mov_b32 s4, 0x3db504f3
	s_cbranch_vccnz .LBB0_14
	v_lshrrev_b32_e32 v18, 2, v126
	v_and_b32_e32 v30, 3, v0
	v_mul_u32_u24_e32 v19, 0x104, v18
	s_movk_i32 s4, 0x1040
	v_mad_u32_u24 v19, v128, s4, v19
	v_lshlrev_b32_e32 v20, 6, v30
	s_mov_b32 s4, 0x11000
	v_add3_u32 v19, v19, v20, s4
	ds_read2_b32 v[20:21], v19 offset1:1
	ds_read2_b32 v[24:25], v19 offset0:2 offset1:3
	ds_read2_b32 v[26:27], v19 offset0:4 offset1:5
	ds_read2_b32 v[28:29], v19 offset0:6 offset1:7
	v_cmp_eq_u32_e32 vcc, 0, v30
	s_waitcnt lgkmcnt(3)
	v_add_f32_e32 v20, 0, v20
	v_add_f32_e32 v20, v20, v21
	s_waitcnt lgkmcnt(2)
	v_add_f32_e32 v20, v20, v24
	v_add_f32_e32 v20, v20, v25
	s_waitcnt lgkmcnt(1)
	v_add_f32_e32 v20, v20, v26
	v_add_f32_e32 v20, v20, v27
	s_waitcnt lgkmcnt(0)
	v_add_f32_e32 v24, v20, v28
	ds_read2_b32 v[20:21], v19 offset0:8 offset1:9
	v_add_f32_e32 v31, v24, v29
	ds_read2_b32 v[24:25], v19 offset0:10 offset1:11
	ds_read2_b32 v[26:27], v19 offset0:12 offset1:13
	ds_read2_b32 v[28:29], v19 offset0:14 offset1:15
	s_waitcnt lgkmcnt(3)
	v_add_f32_e32 v19, v31, v20
	v_add_f32_e32 v19, v19, v21
	s_waitcnt lgkmcnt(2)
	v_add_f32_e32 v19, v19, v24
	v_add_f32_e32 v19, v19, v25
	s_waitcnt lgkmcnt(1)
	v_add_f32_e32 v19, v19, v26
	v_add_f32_e32 v19, v19, v27
	s_waitcnt lgkmcnt(0)
	v_add_f32_e32 v19, v19, v28
	v_add_f32_e32 v19, v19, v29
	s_nop 1
	v_add_f32_dpp v19, v19, v19 quad_perm:[1,0,3,2] row_mask:0xf bank_mask:0xf bound_ctrl:1
	s_nop 1
	v_mov_b32_dpp v109, v19 quad_perm:[2,3,0,1] row_mask:0xf bank_mask:0xf
	s_and_saveexec_b64 s[4:5], vcc
	s_cbranch_execz .LBB0_13
	v_lshlrev_b32_e32 v20, 2, v128
	v_lshlrev_b32_e32 v18, 5, v18
	s_mov_b32 s9, 0x1d600
	v_or3_b32 v18, v20, v18, s9
	v_add_f32_e32 v19, v19, v109
	ds_write_b32 v18, v19

.LBB0_40:
	s_cmpk_gt_i32 s2, 0x7f
	s_cbranch_scc1 .Lp_end
	s_waitcnt vmcnt(9)
	v_mov_b32_e32 v44, 0
	v_cmp_ne_u32_e64 s[46:47], 0, v85
	v_cmp_ne_u32_e64 s[48:49], 0, v84
	v_cmp_ne_u32_e64 s[50:51], 0, v83
	v_cmp_ne_u32_e64 s[52:53], 0, v82
	v_addc_co_u32_e64 v44, s[54:55], v44, v44, s[46:47]
	v_addc_co_u32_e64 v44, s[54:55], v44, v44, s[48:49]
	v_addc_co_u32_e64 v44, s[54:55], v44, v44, s[50:51]
	v_addc_co_u32_e64 v44, s[54:55], v44, v44, s[52:53]
	v_cmp_ne_u32_e64 s[46:47], 0, v81
	v_cmp_ne_u32_e64 s[48:49], 0, v80
	v_cmp_ne_u32_e64 s[50:51], 0, v79
	v_cmp_ne_u32_e64 s[52:53], 0, v78
	v_addc_co_u32_e64 v44, s[54:55], v44, v44, s[46:47]
	v_addc_co_u32_e64 v44, s[54:55], v44, v44, s[48:49]
	v_addc_co_u32_e64 v44, s[54:55], v44, v44, s[50:51]
	v_addc_co_u32_e64 v44, s[54:55], v44, v44, s[52:53]
	v_cmp_ne_u32_e64 s[46:47], 0, v77
	v_cmp_ne_u32_e64 s[48:49], 0, v76
	v_cmp_ne_u32_e64 s[50:51], 0, v75
	v_cmp_ne_u32_e64 s[52:53], 0, v74
	v_addc_co_u32_e64 v44, s[54:55], v44, v44, s[46:47]
	v_addc_co_u32_e64 v44, s[54:55], v44, v44, s[48:49]
	v_addc_co_u32_e64 v44, s[54:55], v44, v44, s[50:51]
	v_addc_co_u32_e64 v44, s[54:55], v44, v44, s[52:53]
	v_cmp_ne_u32_e64 s[46:47], 0, v73
	v_cmp_ne_u32_e64 s[48:49], 0, v72
	v_cmp_ne_u32_e64 s[50:51], 0, v71
	v_cmp_ne_u32_e64 s[52:53], 0, v70
	v_addc_co_u32_e64 v44, s[54:55], v44, v44, s[46:47]
	v_addc_co_u32_e64 v44, s[54:55], v44, v44, s[48:49]
	v_addc_co_u32_e64 v44, s[54:55], v44, v44, s[50:51]
	v_addc_co_u32_e64 v44, s[54:55], v44, v44, s[52:53]
	s_waitcnt vmcnt(5)
	v_mov_b32_e32 v45, 0
	v_cmp_ne_u32_e64 s[46:47], 0, v101
	v_cmp_ne_u32_e64 s[48:49], 0, v100
	v_cmp_ne_u32_e64 s[50:51], 0, v99
	v_cmp_ne_u32_e64 s[52:53], 0, v98
	v_addc_co_u32_e64 v45, s[54:55], v45, v45, s[46:47]
	v_addc_co_u32_e64 v45, s[54:55], v45, v45, s[48:49]
	v_addc_co_u32_e64 v45, s[54:55], v45, v45, s[50:51]
	v_addc_co_u32_e64 v45, s[54:55], v45, v45, s[52:53]
	v_cmp_ne_u32_e64 s[46:47], 0, v97
	v_cmp_ne_u32_e64 s[48:49], 0, v96
	v_cmp_ne_u32_e64 s[50:51], 0, v95
	v_cmp_ne_u32_e64 s[52:53], 0, v94
	v_addc_co_u32_e64 v45, s[54:55], v45, v45, s[46:47]
	v_addc_co_u32_e64 v45, s[54:55], v45, v45, s[48:49]
	v_addc_co_u32_e64 v45, s[54:55], v45, v45, s[50:51]
	v_addc_co_u32_e64 v45, s[54:55], v45, v45, s[52:53]
	v_cmp_ne_u32_e64 s[46:47], 0, v93
	v_cmp_ne_u32_e64 s[48:49], 0, v92
	v_cmp_ne_u32_e64 s[50:51], 0, v91
	v_cmp_ne_u32_e64 s[52:53], 0, v90
	v_addc_co_u32_e64 v45, s[54:55], v45, v45, s[46:47]
	v_addc_co_u32_e64 v45, s[54:55], v45, v45, s[48:49]
	v_addc_co_u32_e64 v45, s[54:55], v45, v45, s[50:51]
	v_addc_co_u32_e64 v45, s[54:55], v45, v45, s[52:53]
	v_cmp_ne_u32_e64 s[46:47], 0, v89
	v_cmp_ne_u32_e64 s[48:49], 0, v88
	v_cmp_ne_u32_e64 s[50:51], 0, v87
	v_cmp_ne_u32_e64 s[52:53], 0, v86
	v_addc_co_u32_e64 v45, s[54:55], v45, v45, s[46:47]
	v_addc_co_u32_e64 v45, s[54:55], v45, v45, s[48:49]
	v_addc_co_u32_e64 v45, s[54:55], v45, v45, s[50:51]
	v_addc_co_u32_e64 v45, s[54:55], v45, v45, s[52:53]
	s_lshl_b32 s13, s2, 4
	v_lshl_add_u32 v46, v128, 1, s13
	v_lshlrev_b32_e32 v46, 7, v46
	v_lshl_add_u32 v46, v126, 1, v46
	global_store_short v46, v44, s[28:29] sc1
	global_store_short v46, v45, s[28:29] offset:128 sc1
